# v21 plus first K fragment reads issued right after the step barrier
# baseline (speedup 1.0000x reference)
.LBB0_536:
	s_or_b32 s6, s58, 1
	s_cmp_ge_u32 s6, s29
	s_waitcnt lgkmcnt(0)
	s_barrier
	s_cselect_b64 s[6:7], -1, 0
	s_mov_b32 s99, 0
	s_cmp_le_i32 s63, s28
	s_cbranch_scc0 .Lnopf_a0b0
	s_cmp_eq_u32 s17, 0
	s_cbranch_scc1 .Lnopf_a0b0
	s_mov_b32 s99, 1
	ds_read_b128 v[116:119], v189 offset:0
	ds_read_b128 v[120:123], v226 offset:0
	ds_read_b128 v[124:127], v227 offset:0
	ds_read_b128 v[128:131], v228 offset:0
.Lnopf_a0b0:
	s_xor_b64 s[56:57], s[18:19], -1
	s_or_b64 s[6:7], s[56:57], s[6:7]
	s_and_b64 vcc, exec, s[6:7]
	s_cbranch_vccnz .LBB0_538
	s_add_u32 s6, s50, 0xfff80000
	s_addc_u32 s7, s51, -1
	s_mov_b32 s40, m0
	s_mov_b32 m0, s68
	s_nop 0
	global_load_lds_dwordx4 v1, s[6:7]
	s_mov_b32 m0, s40
	s_nop 0
	s_mov_b32 s40, m0
	s_mov_b32 m0, s79
	s_nop 0
	global_load_lds_dwordx4 v208, s[6:7]
	s_mov_b32 m0, s40
	s_nop 0
	s_mov_b32 s40, m0
	s_mov_b32 m0, s80
	s_nop 0
	global_load_lds_dwordx4 v209, s[6:7]
	s_mov_b32 m0, s40
	s_nop 0
	s_mov_b32 s40, m0
	s_mov_b32 m0, s81
	s_nop 0
	global_load_lds_dwordx4 v210, s[6:7]
	s_mov_b32 m0, s40
	s_add_u32 s6, s54, 0xffffe000
	s_addc_u32 s7, s55, -1
	s_mov_b32 s40, m0
	s_mov_b32 m0, s69
	s_nop 0
	global_load_lds_dwordx4 v188, s[6:7]
	s_mov_b32 m0, s40
	s_nop 0
	s_mov_b32 s40, m0
	s_mov_b32 m0, s82
	s_nop 0
	global_load_lds_dwordx4 v211, s[6:7]
	s_mov_b32 m0, s40
	s_add_u32 s6, s52, 0xfff80000
	s_addc_u32 s7, s53, -1
	s_mov_b32 s40, m0
	s_mov_b32 m0, s70
	s_nop 0
	global_load_lds_dwordx4 v181, s[6:7]
	s_mov_b32 m0, s40
	s_nop 0
	s_mov_b32 s40, m0
	s_mov_b32 m0, s83
	s_nop 0
	global_load_lds_dwordx4 v212, s[6:7]
	s_mov_b32 m0, s40
	s_nop 0
	s_mov_b32 s40, m0
	s_mov_b32 m0, s84
	s_nop 0
	global_load_lds_dwordx4 v213, s[6:7]
	s_mov_b32 m0, s40
	s_nop 0
	s_mov_b32 s40, m0
	s_mov_b32 m0, s85
	s_nop 0
	global_load_lds_dwordx4 v214, s[6:7]
	s_mov_b32 m0, s40

.LBB0_544:
	s_add_i32 s58, s58, 2
	s_cmp_ge_u32 s58, s29
	s_cselect_b64 s[8:9], -1, 0
	s_cmp_lt_u32 s58, s29
	s_waitcnt lgkmcnt(0)
	s_barrier
	s_cselect_b64 s[40:41], -1, 0
	s_mov_b32 s99, 0
	s_add_i32 s98, s63, 64
	s_cmp_le_i32 s98, s28
	s_cbranch_scc0 .Lnopf_a0b1
	s_mov_b32 s99, 1
	ds_read_b128 v[116:119], v189 offset:24576
	ds_read_b128 v[120:123], v226 offset:24576
	ds_read_b128 v[124:127], v227 offset:24576
	ds_read_b128 v[128:131], v228 offset:24576
.Lnopf_a0b1:
	s_and_b64 s[40:41], s[18:19], s[40:41]
	s_andn2_b64 vcc, exec, s[40:41]
	s_cbranch_vccnz .LBB0_546
	s_mov_b32 s15, m0
	s_mov_b32 m0, s65
	s_nop 0
	global_load_lds_dwordx4 v1, s[50:51]
	s_mov_b32 m0, s15
	s_nop 0
	s_mov_b32 s15, m0
	s_mov_b32 m0, s73
	s_nop 0
	global_load_lds_dwordx4 v208, s[50:51]
	s_mov_b32 m0, s15
	s_nop 0
	s_mov_b32 s15, m0
	s_mov_b32 m0, s74
	s_nop 0
	global_load_lds_dwordx4 v209, s[50:51]
	s_mov_b32 m0, s15
	s_nop 0
	s_mov_b32 s15, m0
	s_mov_b32 m0, s75
	s_nop 0
	global_load_lds_dwordx4 v210, s[50:51]
	s_mov_b32 m0, s15
	s_nop 0
	s_mov_b32 s15, m0
	s_mov_b32 m0, s66
	s_nop 0
	global_load_lds_dwordx4 v188, s[54:55]
	s_mov_b32 m0, s15
	s_nop 0
	s_mov_b32 s15, m0
	s_mov_b32 m0, s76
	s_nop 0
	global_load_lds_dwordx4 v211, s[54:55]
	s_mov_b32 m0, s15
	s_nop 0
	s_mov_b32 s15, m0
	s_mov_b32 m0, s67
	s_nop 0
	global_load_lds_dwordx4 v181, s[52:53]
	s_mov_b32 m0, s15
	s_nop 0
	s_mov_b32 s15, m0
	s_mov_b32 m0, s64
	s_nop 0
	global_load_lds_dwordx4 v212, s[52:53]
	s_mov_b32 m0, s15
	s_nop 0
	s_mov_b32 s15, m0
	s_mov_b32 m0, s77
	s_nop 0
	global_load_lds_dwordx4 v213, s[52:53]
	s_mov_b32 m0, s15
	s_nop 0
	s_mov_b32 s15, m0
	s_mov_b32 m0, s78
	s_nop 0
	global_load_lds_dwordx4 v214, s[52:53]
	s_mov_b32 m0, s15

.LBB0_556:
	s_cmp_eq_u32 s99, 1
	s_cbranch_scc0 .Lorig_a0b0
	s_setprio 3
	s_waitcnt lgkmcnt(3)
	v_mfma_f32_32x32x16_bf16 v[84:99], v[116:119], v[132:135], 0
	ds_read_b128 v[116:119], v232 offset:0
	s_waitcnt lgkmcnt(3)
	v_mfma_f32_32x32x16_bf16 v[84:99], v[120:123], v[136:139], v[84:99]
	ds_read_b128 v[120:123], v233 offset:0
	s_waitcnt lgkmcnt(3)
	v_mfma_f32_32x32x16_bf16 v[84:99], v[124:127], v[140:143], v[84:99]
	ds_read_b128 v[124:127], v234 offset:0
	s_waitcnt lgkmcnt(3)
	v_mfma_f32_32x32x16_bf16 v[84:99], v[128:131], v[144:147], v[84:99]
	ds_read_b128 v[128:131], v235 offset:0
	s_waitcnt lgkmcnt(3)
	v_mfma_f32_32x32x16_bf16 v[84:99], v[116:119], v[148:151], v[84:99]
	ds_read_b128 v[116:119], v190 offset:0
	s_waitcnt lgkmcnt(3)
	v_mfma_f32_32x32x16_bf16 v[84:99], v[120:123], v[152:155], v[84:99]
	ds_read_b128 v[120:123], v229 offset:0
	s_waitcnt lgkmcnt(3)
	v_mfma_f32_32x32x16_bf16 v[84:99], v[124:127], v[156:159], v[84:99]
	ds_read_b128 v[124:127], v230 offset:0
	s_waitcnt lgkmcnt(3)
	v_mfma_f32_32x32x16_bf16 v[84:99], v[128:131], v[160:163], v[84:99]
	ds_read_b128 v[128:131], v231 offset:0
	s_waitcnt lgkmcnt(3)
	v_mfma_f32_32x32x16_bf16 v[84:99], v[116:119], v[164:167], v[84:99]
	ds_read_b128 v[116:119], v189 offset:8192
	s_waitcnt lgkmcnt(3)
	v_mfma_f32_32x32x16_bf16 v[84:99], v[120:123], v[172:175], v[84:99]
	ds_read_b128 v[120:123], v226 offset:8192
	s_waitcnt lgkmcnt(3)
	v_mfma_f32_32x32x16_bf16 v[84:99], v[124:127], v[168:171], v[84:99]
	ds_read_b128 v[124:127], v227 offset:8192
	s_waitcnt lgkmcnt(3)
	v_mfma_f32_32x32x16_bf16 v[84:99], v[128:131], v[176:179], v[84:99]
	ds_read_b128 v[128:131], v228 offset:8192
	s_waitcnt lgkmcnt(3)
	v_mfma_f32_32x32x16_bf16 v[68:83], v[116:119], v[132:135], 0
	ds_read_b128 v[116:119], v232 offset:8192
	s_waitcnt lgkmcnt(3)
	v_mfma_f32_32x32x16_bf16 v[68:83], v[120:123], v[136:139], v[68:83]
	ds_read_b128 v[120:123], v233 offset:8192
	s_waitcnt lgkmcnt(3)
	v_mfma_f32_32x32x16_bf16 v[68:83], v[124:127], v[140:143], v[68:83]
	ds_read_b128 v[124:127], v234 offset:8192
	s_waitcnt lgkmcnt(3)
	v_mfma_f32_32x32x16_bf16 v[68:83], v[128:131], v[144:147], v[68:83]
	ds_read_b128 v[128:131], v235 offset:8192
	s_waitcnt lgkmcnt(3)
	v_mfma_f32_32x32x16_bf16 v[68:83], v[116:119], v[148:151], v[68:83]
	ds_read_b128 v[116:119], v190 offset:4096
	s_waitcnt lgkmcnt(3)
	v_mfma_f32_32x32x16_bf16 v[68:83], v[120:123], v[152:155], v[68:83]
	ds_read_b128 v[120:123], v229 offset:4096
	s_waitcnt lgkmcnt(3)
	v_mfma_f32_32x32x16_bf16 v[68:83], v[124:127], v[156:159], v[68:83]
	ds_read_b128 v[124:127], v230 offset:4096
	s_waitcnt lgkmcnt(3)
	v_mfma_f32_32x32x16_bf16 v[68:83], v[128:131], v[160:163], v[68:83]
	ds_read_b128 v[128:131], v231 offset:4096
	s_waitcnt lgkmcnt(3)
	v_mfma_f32_32x32x16_bf16 v[68:83], v[116:119], v[164:167], v[68:83]
	s_waitcnt lgkmcnt(2)
	v_mfma_f32_32x32x16_bf16 v[68:83], v[120:123], v[172:175], v[68:83]
	s_waitcnt lgkmcnt(1)
	v_mfma_f32_32x32x16_bf16 v[68:83], v[124:127], v[168:171], v[68:83]
	s_waitcnt lgkmcnt(0)
	v_mfma_f32_32x32x16_bf16 v[68:83], v[128:131], v[176:179], v[68:83]
	ds_read_b64_tr_b16 v[116:117], v191 offset:0
	ds_read_b64_tr_b16 v[118:119], v191 offset:2048
	ds_read_b64_tr_b16 v[120:121], v191 offset:4096
	ds_read_b64_tr_b16 v[122:123], v191 offset:6144
	ds_read_b64_tr_b16 v[124:125], v191 offset:8192
	ds_read_b64_tr_b16 v[126:127], v191 offset:10240
	ds_read_b64_tr_b16 v[128:129], v191 offset:12288
	ds_read_b64_tr_b16 v[130:131], v191 offset:14336
	s_setprio 0
	s_nop 7
	s_nop 3
	v_cmp_eq_f32_e32 vcc, 0, v223
	s_cmp_eq_u64 vcc, exec
	s_cbranch_scc0 .Lsub_a0b0
	v_exp_f32_e32 v100, v84
	v_exp_f32_e32 v101, v85
	v_exp_f32_e32 v102, v86
	v_exp_f32_e32 v103, v87
	v_exp_f32_e32 v104, v88
	v_exp_f32_e32 v105, v89
	v_exp_f32_e32 v106, v90
	v_exp_f32_e32 v107, v91
	v_exp_f32_e32 v108, v92
	v_exp_f32_e32 v109, v93
	v_exp_f32_e32 v110, v94
	v_exp_f32_e32 v111, v95
	v_exp_f32_e32 v112, v96
	v_exp_f32_e32 v113, v97
	v_exp_f32_e32 v114, v98
	v_exp_f32_e32 v115, v99
	v_add_f32_e32 v237, v100, v101
	v_add_f32_e32 v251, v102, v103
	v_add_f32_e32 v237, v237, v104
	v_add_f32_e32 v251, v251, v105
	v_add_f32_e32 v237, v237, v106
	v_add_f32_e32 v251, v251, v107
	v_add_f32_e32 v237, v237, v108
	v_add_f32_e32 v251, v251, v109
	v_add_f32_e32 v237, v237, v110
	v_add_f32_e32 v251, v251, v111
	v_add_f32_e32 v237, v237, v112
	v_add_f32_e32 v251, v251, v113
	v_add_f32_e32 v237, v237, v114
	v_add_f32_e32 v251, v251, v115
	v_add_f32_e32 v237, v237, v251
	v_cvt_pk_bf16_f32 v238, v100, v101
	v_cvt_pk_bf16_f32 v239, v102, v103
	v_cvt_pk_bf16_f32 v240, v104, v105
	v_cvt_pk_bf16_f32 v241, v106, v107
	v_cvt_pk_bf16_f32 v242, v108, v109
	v_cvt_pk_bf16_f32 v243, v110, v111
	v_cvt_pk_bf16_f32 v244, v112, v113
	v_cvt_pk_bf16_f32 v245, v114, v115
	s_nop 1
	v_permlane32_swap_b32_e32 v238, v240
	v_permlane32_swap_b32_e32 v239, v241
	v_permlane32_swap_b32_e32 v242, v244
	v_permlane32_swap_b32_e32 v243, v245
	v_exp_f32_e32 v100, v68
	v_exp_f32_e32 v101, v69
	v_exp_f32_e32 v102, v70
	v_exp_f32_e32 v103, v71
	v_exp_f32_e32 v104, v72
	v_exp_f32_e32 v105, v73
	v_exp_f32_e32 v106, v74
	v_exp_f32_e32 v107, v75
	v_exp_f32_e32 v108, v76
	v_exp_f32_e32 v109, v77
	v_exp_f32_e32 v110, v78
	v_exp_f32_e32 v111, v79
	v_exp_f32_e32 v112, v80
	v_exp_f32_e32 v113, v81
	v_exp_f32_e32 v114, v82
	v_exp_f32_e32 v115, v83
	v_add_f32_e32 v250, v100, v101
	v_add_f32_e32 v251, v102, v103
	v_add_f32_e32 v250, v250, v104
	v_add_f32_e32 v251, v251, v105
	v_add_f32_e32 v250, v250, v106
	v_add_f32_e32 v251, v251, v107
	v_add_f32_e32 v250, v250, v108
	v_add_f32_e32 v251, v251, v109
	v_add_f32_e32 v250, v250, v110
	v_add_f32_e32 v251, v251, v111
	v_add_f32_e32 v250, v250, v112
	v_add_f32_e32 v251, v251, v113
	v_add_f32_e32 v250, v250, v114
	v_add_f32_e32 v251, v251, v115
	v_add_f32_e32 v250, v250, v251
	v_cvt_pk_bf16_f32 v100, v100, v101
	v_cvt_pk_bf16_f32 v101, v102, v103
	v_cvt_pk_bf16_f32 v102, v104, v105
	v_cvt_pk_bf16_f32 v103, v106, v107
	v_cvt_pk_bf16_f32 v104, v108, v109
	v_cvt_pk_bf16_f32 v105, v110, v111
	v_cvt_pk_bf16_f32 v106, v112, v113
	v_cvt_pk_bf16_f32 v107, v114, v115
	s_nop 1
	v_permlane32_swap_b32_e32 v100, v102
	v_permlane32_swap_b32_e32 v101, v103
	v_permlane32_swap_b32_e32 v104, v106
	v_permlane32_swap_b32_e32 v105, v107
	s_branch .Lsum_a0b0

.LBB0_571:
	s_cmp_eq_u32 s99, 1
	s_cbranch_scc0 .Lorig_a0b1
	s_setprio 3
	s_waitcnt lgkmcnt(3)
	v_mfma_f32_32x32x16_bf16 v[84:99], v[116:119], v[132:135], 0
	ds_read_b128 v[116:119], v232 offset:24576
	s_waitcnt lgkmcnt(3)
	v_mfma_f32_32x32x16_bf16 v[84:99], v[120:123], v[136:139], v[84:99]
	ds_read_b128 v[120:123], v233 offset:24576
	s_waitcnt lgkmcnt(3)
	v_mfma_f32_32x32x16_bf16 v[84:99], v[124:127], v[140:143], v[84:99]
	ds_read_b128 v[124:127], v234 offset:24576
	s_waitcnt lgkmcnt(3)
	v_mfma_f32_32x32x16_bf16 v[84:99], v[128:131], v[144:147], v[84:99]
	ds_read_b128 v[128:131], v235 offset:24576
	s_waitcnt lgkmcnt(3)
	v_mfma_f32_32x32x16_bf16 v[84:99], v[116:119], v[148:151], v[84:99]
	ds_read_b128 v[116:119], v190 offset:24576
	s_waitcnt lgkmcnt(3)
	v_mfma_f32_32x32x16_bf16 v[84:99], v[120:123], v[152:155], v[84:99]
	ds_read_b128 v[120:123], v229 offset:24576
	s_waitcnt lgkmcnt(3)
	v_mfma_f32_32x32x16_bf16 v[84:99], v[124:127], v[156:159], v[84:99]
	ds_read_b128 v[124:127], v230 offset:24576
	s_waitcnt lgkmcnt(3)
	v_mfma_f32_32x32x16_bf16 v[84:99], v[128:131], v[160:163], v[84:99]
	ds_read_b128 v[128:131], v231 offset:24576
	s_waitcnt lgkmcnt(3)
	v_mfma_f32_32x32x16_bf16 v[84:99], v[116:119], v[164:167], v[84:99]
	ds_read_b128 v[116:119], v189 offset:32768
	s_waitcnt lgkmcnt(3)
	v_mfma_f32_32x32x16_bf16 v[84:99], v[120:123], v[172:175], v[84:99]
	ds_read_b128 v[120:123], v226 offset:32768
	s_waitcnt lgkmcnt(3)
	v_mfma_f32_32x32x16_bf16 v[84:99], v[124:127], v[168:171], v[84:99]
	ds_read_b128 v[124:127], v227 offset:32768
	s_waitcnt lgkmcnt(3)
	v_mfma_f32_32x32x16_bf16 v[84:99], v[128:131], v[176:179], v[84:99]
	ds_read_b128 v[128:131], v228 offset:32768
	s_waitcnt lgkmcnt(3)
	v_mfma_f32_32x32x16_bf16 v[68:83], v[116:119], v[132:135], 0
	ds_read_b128 v[116:119], v232 offset:32768
	s_waitcnt lgkmcnt(3)
	v_mfma_f32_32x32x16_bf16 v[68:83], v[120:123], v[136:139], v[68:83]
	ds_read_b128 v[120:123], v233 offset:32768
	s_waitcnt lgkmcnt(3)
	v_mfma_f32_32x32x16_bf16 v[68:83], v[124:127], v[140:143], v[68:83]
	ds_read_b128 v[124:127], v234 offset:32768
	s_waitcnt lgkmcnt(3)
	v_mfma_f32_32x32x16_bf16 v[68:83], v[128:131], v[144:147], v[68:83]
	ds_read_b128 v[128:131], v235 offset:32768
	s_waitcnt lgkmcnt(3)
	v_mfma_f32_32x32x16_bf16 v[68:83], v[116:119], v[148:151], v[68:83]
	ds_read_b128 v[116:119], v190 offset:28672
	s_waitcnt lgkmcnt(3)
	v_mfma_f32_32x32x16_bf16 v[68:83], v[120:123], v[152:155], v[68:83]
	ds_read_b128 v[120:123], v229 offset:28672
	s_waitcnt lgkmcnt(3)
	v_mfma_f32_32x32x16_bf16 v[68:83], v[124:127], v[156:159], v[68:83]
	ds_read_b128 v[124:127], v230 offset:28672
	s_waitcnt lgkmcnt(3)
	v_mfma_f32_32x32x16_bf16 v[68:83], v[128:131], v[160:163], v[68:83]
	ds_read_b128 v[128:131], v231 offset:28672
	s_waitcnt lgkmcnt(3)
	v_mfma_f32_32x32x16_bf16 v[68:83], v[116:119], v[164:167], v[68:83]
	s_waitcnt lgkmcnt(2)
	v_mfma_f32_32x32x16_bf16 v[68:83], v[120:123], v[172:175], v[68:83]
	s_waitcnt lgkmcnt(1)
	v_mfma_f32_32x32x16_bf16 v[68:83], v[124:127], v[168:171], v[68:83]
	s_waitcnt lgkmcnt(0)
	v_mfma_f32_32x32x16_bf16 v[68:83], v[128:131], v[176:179], v[68:83]
	ds_read_b64_tr_b16 v[116:117], v191 offset:16384
	ds_read_b64_tr_b16 v[118:119], v191 offset:18432
	ds_read_b64_tr_b16 v[120:121], v191 offset:20480
	ds_read_b64_tr_b16 v[122:123], v191 offset:22528
	ds_read_b64_tr_b16 v[124:125], v191 offset:24576
	ds_read_b64_tr_b16 v[126:127], v191 offset:26624
	ds_read_b64_tr_b16 v[128:129], v191 offset:28672
	ds_read_b64_tr_b16 v[130:131], v191 offset:30720
	s_setprio 0
	s_nop 7
	s_nop 3
	v_cmp_eq_f32_e32 vcc, 0, v222
	s_cmp_eq_u64 vcc, exec
	s_cbranch_scc0 .Lsub_a0b1
	v_exp_f32_e32 v100, v84
	v_exp_f32_e32 v101, v85
	v_exp_f32_e32 v102, v86
	v_exp_f32_e32 v103, v87
	v_exp_f32_e32 v104, v88
	v_exp_f32_e32 v105, v89
	v_exp_f32_e32 v106, v90
	v_exp_f32_e32 v107, v91
	v_exp_f32_e32 v108, v92
	v_exp_f32_e32 v109, v93
	v_exp_f32_e32 v110, v94
	v_exp_f32_e32 v111, v95
	v_exp_f32_e32 v112, v96
	v_exp_f32_e32 v113, v97
	v_exp_f32_e32 v114, v98
	v_exp_f32_e32 v115, v99
	v_add_f32_e32 v237, v100, v101
	v_add_f32_e32 v251, v102, v103
	v_add_f32_e32 v237, v237, v104
	v_add_f32_e32 v251, v251, v105
	v_add_f32_e32 v237, v237, v106
	v_add_f32_e32 v251, v251, v107
	v_add_f32_e32 v237, v237, v108
	v_add_f32_e32 v251, v251, v109
	v_add_f32_e32 v237, v237, v110
	v_add_f32_e32 v251, v251, v111
	v_add_f32_e32 v237, v237, v112
	v_add_f32_e32 v251, v251, v113
	v_add_f32_e32 v237, v237, v114
	v_add_f32_e32 v251, v251, v115
	v_add_f32_e32 v237, v237, v251
	v_cvt_pk_bf16_f32 v238, v100, v101
	v_cvt_pk_bf16_f32 v239, v102, v103
	v_cvt_pk_bf16_f32 v240, v104, v105
	v_cvt_pk_bf16_f32 v241, v106, v107
	v_cvt_pk_bf16_f32 v242, v108, v109
	v_cvt_pk_bf16_f32 v243, v110, v111
	v_cvt_pk_bf16_f32 v244, v112, v113
	v_cvt_pk_bf16_f32 v245, v114, v115
	s_nop 1
	v_permlane32_swap_b32_e32 v238, v240
	v_permlane32_swap_b32_e32 v239, v241
	v_permlane32_swap_b32_e32 v242, v244
	v_permlane32_swap_b32_e32 v243, v245
	v_exp_f32_e32 v100, v68
	v_exp_f32_e32 v101, v69
	v_exp_f32_e32 v102, v70
	v_exp_f32_e32 v103, v71
	v_exp_f32_e32 v104, v72
	v_exp_f32_e32 v105, v73
	v_exp_f32_e32 v106, v74
	v_exp_f32_e32 v107, v75
	v_exp_f32_e32 v108, v76
	v_exp_f32_e32 v109, v77
	v_exp_f32_e32 v110, v78
	v_exp_f32_e32 v111, v79
	v_exp_f32_e32 v112, v80
	v_exp_f32_e32 v113, v81
	v_exp_f32_e32 v114, v82
	v_exp_f32_e32 v115, v83
	v_add_f32_e32 v250, v100, v101
	v_add_f32_e32 v251, v102, v103
	v_add_f32_e32 v250, v250, v104
	v_add_f32_e32 v251, v251, v105
	v_add_f32_e32 v250, v250, v106
	v_add_f32_e32 v251, v251, v107
	v_add_f32_e32 v250, v250, v108
	v_add_f32_e32 v251, v251, v109
	v_add_f32_e32 v250, v250, v110
	v_add_f32_e32 v251, v251, v111
	v_add_f32_e32 v250, v250, v112
	v_add_f32_e32 v251, v251, v113
	v_add_f32_e32 v250, v250, v114
	v_add_f32_e32 v251, v251, v115
	v_add_f32_e32 v250, v250, v251
	v_cvt_pk_bf16_f32 v100, v100, v101
	v_cvt_pk_bf16_f32 v101, v102, v103
	v_cvt_pk_bf16_f32 v102, v104, v105
	v_cvt_pk_bf16_f32 v103, v106, v107
	v_cvt_pk_bf16_f32 v104, v108, v109
	v_cvt_pk_bf16_f32 v105, v110, v111
	v_cvt_pk_bf16_f32 v106, v112, v113
	v_cvt_pk_bf16_f32 v107, v114, v115
	s_nop 1
	v_permlane32_swap_b32_e32 v100, v102
	v_permlane32_swap_b32_e32 v101, v103
	v_permlane32_swap_b32_e32 v104, v106
	v_permlane32_swap_b32_e32 v105, v107
	s_branch .Lsum_a0b1

.LBB0_1430:
	s_or_b32 s8, s19, 1
	s_cmp_ge_u32 s8, s41
	s_waitcnt lgkmcnt(0)
	s_barrier
	s_cselect_b64 s[8:9], -1, 0
	s_mov_b32 s99, 0
	s_cmp_le_i32 s18, s40
	s_cbranch_scc0 .Lnopf_a1b0
	s_cmp_eq_u32 s71, 0
	s_cbranch_scc1 .Lnopf_a1b0
	s_mov_b32 s99, 1
	ds_read_b128 v[208:211], v172 offset:32768
	ds_read_b128 v[212:215], v206 offset:32768
	ds_read_b128 v[216:219], v207 offset:32768
	ds_read_b128 v[220:223], v237 offset:32768
	ds_read_b128 v[224:227], v244 offset:32768
	ds_read_b128 v[228:231], v245 offset:32768
	ds_read_b128 v[232:235], v246 offset:32768
	ds_read_b128 v[238:241], v247 offset:32768
.Lnopf_a1b0:
	s_xor_b64 s[58:59], s[20:21], -1
	s_or_b64 s[8:9], s[58:59], s[8:9]
	s_and_b64 vcc, exec, s[8:9]
	s_cbranch_vccnz .LBB0_1433
	s_add_u32 s8, s54, 0xfff00000
	s_addc_u32 s9, s55, -1
	s_mov_b32 s42, m0
	s_mov_b32 m0, s79
	s_nop 0
	global_load_lds_dwordx4 v1, s[8:9]
	s_mov_b32 m0, s42
	s_nop 0
	s_mov_b32 s42, m0
	s_mov_b32 m0, s89
	s_nop 0
	global_load_lds_dwordx4 v178, s[8:9]
	s_mov_b32 m0, s42
	s_nop 0
	s_mov_b32 s42, m0
	s_mov_b32 m0, s90
	s_nop 0
	global_load_lds_dwordx4 v179, s[8:9]
	s_mov_b32 m0, s42
	s_nop 0
	s_mov_b32 s42, m0
	s_mov_b32 m0, s91
	s_nop 0
	global_load_lds_dwordx4 v180, s[8:9]
	s_mov_b32 m0, s42
	s_add_u32 s8, s56, 0xfff00000
	s_addc_u32 s9, s57, -1
	s_mov_b32 s42, m0
	s_mov_b32 m0, s80
	s_nop 0
	global_load_lds_dwordx4 v133, s[8:9]
	s_mov_b32 m0, s42
	s_and_b64 vcc, exec, s[6:7]
	s_mov_b32 s42, m0
	s_mov_b32 m0, s92
	s_nop 0
	global_load_lds_dwordx4 v181, s[8:9]
	s_mov_b32 m0, s42
	s_nop 0
	s_mov_b32 s42, m0
	s_mov_b32 m0, s93
	s_nop 0
	global_load_lds_dwordx4 v182, s[8:9]
	s_mov_b32 m0, s42
	s_nop 0
	s_mov_b32 s42, m0
	s_mov_b32 m0, s94
	s_nop 0
	global_load_lds_dwordx4 v183, s[8:9]
	s_mov_b32 m0, s42
	s_cbranch_vccnz .LBB0_1433
	s_add_u32 s8, s52, 0xffffff00
	s_addc_u32 s9, s53, -1
	s_mov_b32 s42, m0
	s_mov_b32 m0, s83
	s_nop 0
	global_load_lds_dword v175, s[8:9]
	s_mov_b32 m0, s42

.LBB0_1439:
	s_add_i32 s19, s19, 2
	s_cmp_ge_u32 s19, s41
	s_cselect_b64 s[10:11], -1, 0
	s_cmp_lt_u32 s19, s41
	s_waitcnt lgkmcnt(0)
	s_barrier
	s_cselect_b64 s[42:43], -1, 0
	s_mov_b32 s99, 0
	s_add_i32 s98, s18, 64
	s_cmp_le_i32 s98, s40
	s_cbranch_scc0 .Lnopf_a1b1
	s_mov_b32 s99, 1
	ds_read_b128 v[208:211], v172 offset:49152
	ds_read_b128 v[212:215], v206 offset:49152
	ds_read_b128 v[216:219], v207 offset:49152
	ds_read_b128 v[220:223], v237 offset:49152
	ds_read_b128 v[224:227], v244 offset:49152
	ds_read_b128 v[228:231], v245 offset:49152
	ds_read_b128 v[232:235], v246 offset:49152
	ds_read_b128 v[238:241], v247 offset:49152
.Lnopf_a1b1:
	s_and_b64 s[42:43], s[20:21], s[42:43]
	s_andn2_b64 vcc, exec, s[42:43]
	s_cbranch_vccnz .LBB0_1442
	s_mov_b32 s42, m0
	s_mov_b32 m0, s77
	s_nop 0
	global_load_lds_dwordx4 v1, s[54:55]
	s_mov_b32 m0, s42
	s_and_b64 vcc, exec, s[6:7]
	s_mov_b32 s42, m0
	s_mov_b32 m0, s84
	s_nop 0
	global_load_lds_dwordx4 v178, s[54:55]
	s_mov_b32 m0, s42
	s_nop 0
	s_mov_b32 s42, m0
	s_mov_b32 m0, s85
	s_nop 0
	global_load_lds_dwordx4 v179, s[54:55]
	s_mov_b32 m0, s42
	s_nop 0
	s_mov_b32 s42, m0
	s_mov_b32 m0, s86
	s_nop 0
	global_load_lds_dwordx4 v180, s[54:55]
	s_mov_b32 m0, s42
	s_nop 0
	s_mov_b32 s42, m0
	s_mov_b32 m0, s78
	s_nop 0
	global_load_lds_dwordx4 v133, s[56:57]
	s_mov_b32 m0, s42
	s_nop 0
	s_mov_b32 s42, m0
	s_mov_b32 m0, s76
	s_nop 0
	global_load_lds_dwordx4 v181, s[56:57]
	s_mov_b32 m0, s42
	s_nop 0
	s_mov_b32 s42, m0
	s_mov_b32 m0, s87
	s_nop 0
	global_load_lds_dwordx4 v182, s[56:57]
	s_mov_b32 m0, s42
	s_nop 0
	s_mov_b32 s42, m0
	s_mov_b32 m0, s88
	s_nop 0
	global_load_lds_dwordx4 v183, s[56:57]
	s_mov_b32 m0, s42
	s_cbranch_vccnz .LBB0_1442
	s_mov_b32 s42, m0
	s_mov_b32 m0, s81
	s_nop 0
	global_load_lds_dword v175, s[52:53]
	s_mov_b32 m0, s42

.LBB0_1452:
	s_cmp_eq_u32 s99, 1
	s_cbranch_scc0 .Lorig_a1b0
	s_setprio 3
	ds_read_b128 v[140:143], v176
	ds_read_b128 v[144:147], v176 offset:32
	ds_read_b128 v[148:151], v176 offset:64
	ds_read_b128 v[152:155], v176 offset:96
	ds_read_b128 v[156:159], v176 offset:128
	ds_read_b128 v[160:163], v176 offset:160
	ds_read_b128 v[164:167], v176 offset:192
	ds_read_b128 v[168:171], v176 offset:224
	s_waitcnt lgkmcnt(4)
	v_mfma_f32_32x32x16_bf16 v[84:99], v[208:211], v[100:103], v[140:155]
	ds_read_b128 v[208:211], v172 offset:40960
	s_waitcnt lgkmcnt(15)
	v_mfma_f32_32x32x16_bf16 v[84:99], v[212:215], v[104:107], v[84:99]
	ds_read_b128 v[212:215], v206 offset:40960
	s_waitcnt lgkmcnt(15)
	v_mfma_f32_32x32x16_bf16 v[84:99], v[216:219], v[108:111], v[84:99]
	ds_read_b128 v[216:219], v207 offset:40960
	s_waitcnt lgkmcnt(15)
	v_mfma_f32_32x32x16_bf16 v[84:99], v[220:223], v[112:115], v[84:99]
	ds_read_b128 v[220:223], v237 offset:40960
	s_waitcnt lgkmcnt(15)
	v_mfma_f32_32x32x16_bf16 v[84:99], v[224:227], v[116:119], v[84:99]
	ds_read_b128 v[224:227], v244 offset:40960
	s_waitcnt lgkmcnt(15)
	v_mfma_f32_32x32x16_bf16 v[84:99], v[228:231], v[120:123], v[84:99]
	ds_read_b128 v[228:231], v245 offset:40960
	s_waitcnt lgkmcnt(15)
	v_mfma_f32_32x32x16_bf16 v[84:99], v[232:235], v[124:127], v[84:99]
	ds_read_b128 v[232:235], v246 offset:40960
	s_waitcnt lgkmcnt(15)
	v_mfma_f32_32x32x16_bf16 v[84:99], v[238:241], v[128:131], v[84:99]
	ds_read_b128 v[238:241], v247 offset:40960
	s_waitcnt lgkmcnt(7)
	v_mfma_f32_32x32x16_bf16 v[68:83], v[208:211], v[100:103], v[156:171]
	s_waitcnt lgkmcnt(6)
	v_mfma_f32_32x32x16_bf16 v[68:83], v[212:215], v[104:107], v[68:83]
	s_waitcnt lgkmcnt(5)
	v_mfma_f32_32x32x16_bf16 v[68:83], v[216:219], v[108:111], v[68:83]
	s_waitcnt lgkmcnt(4)
	v_mfma_f32_32x32x16_bf16 v[68:83], v[220:223], v[112:115], v[68:83]
	s_waitcnt lgkmcnt(3)
	v_mfma_f32_32x32x16_bf16 v[68:83], v[224:227], v[116:119], v[68:83]
	s_waitcnt lgkmcnt(2)
	v_mfma_f32_32x32x16_bf16 v[68:83], v[228:231], v[120:123], v[68:83]
	s_waitcnt lgkmcnt(1)
	v_mfma_f32_32x32x16_bf16 v[68:83], v[232:235], v[124:127], v[68:83]
	s_waitcnt lgkmcnt(0)
	v_mfma_f32_32x32x16_bf16 v[68:83], v[238:241], v[128:131], v[68:83]
	ds_read_b64_tr_b16 v[208:209], v174 offset:0
	ds_read_b64_tr_b16 v[210:211], v174 offset:2048
	ds_read_b64_tr_b16 v[212:213], v174 offset:4096
	ds_read_b64_tr_b16 v[214:215], v174 offset:6144
	ds_read_b64_tr_b16 v[216:217], v174 offset:8192
	ds_read_b64_tr_b16 v[218:219], v174 offset:10240
	ds_read_b64_tr_b16 v[220:221], v174 offset:12288
	ds_read_b64_tr_b16 v[222:223], v174 offset:14336
	s_setprio 0
	s_nop 7
	s_nop 3
	v_cmp_eq_f32_e32 vcc, 0, v193
	s_cmp_eq_u64 vcc, exec
	s_cbranch_scc0 .Lsub_a1b0
	v_exp_f32_e32 v140, v84
	v_exp_f32_e32 v141, v85
	v_exp_f32_e32 v142, v86
	v_exp_f32_e32 v143, v87
	v_exp_f32_e32 v144, v88
	v_exp_f32_e32 v145, v89
	v_exp_f32_e32 v146, v90
	v_exp_f32_e32 v147, v91
	v_exp_f32_e32 v148, v92
	v_exp_f32_e32 v149, v93
	v_exp_f32_e32 v150, v94
	v_exp_f32_e32 v151, v95
	v_exp_f32_e32 v152, v96
	v_exp_f32_e32 v153, v97
	v_exp_f32_e32 v154, v98
	v_exp_f32_e32 v155, v99
	v_add_f32_e32 v248, v140, v141
	v_add_f32_e32 v250, v142, v143
	v_add_f32_e32 v248, v248, v144
	v_add_f32_e32 v250, v250, v145
	v_add_f32_e32 v248, v248, v146
	v_add_f32_e32 v250, v250, v147
	v_add_f32_e32 v248, v248, v148
	v_add_f32_e32 v250, v250, v149
	v_add_f32_e32 v248, v248, v150
	v_add_f32_e32 v250, v250, v151
	v_add_f32_e32 v248, v248, v152
	v_add_f32_e32 v250, v250, v153
	v_add_f32_e32 v248, v248, v154
	v_add_f32_e32 v250, v250, v155
	v_add_f32_e32 v248, v248, v250
	v_cvt_pk_bf16_f32 v140, v140, v141
	v_cvt_pk_bf16_f32 v141, v142, v143
	v_cvt_pk_bf16_f32 v142, v144, v145
	v_cvt_pk_bf16_f32 v143, v146, v147
	v_cvt_pk_bf16_f32 v144, v148, v149
	v_cvt_pk_bf16_f32 v145, v150, v151
	v_cvt_pk_bf16_f32 v146, v152, v153
	v_cvt_pk_bf16_f32 v147, v154, v155
	s_nop 1
	v_permlane32_swap_b32_e32 v140, v142
	v_permlane32_swap_b32_e32 v141, v143
	v_permlane32_swap_b32_e32 v144, v146
	v_permlane32_swap_b32_e32 v145, v147
	v_exp_f32_e32 v156, v68
	v_exp_f32_e32 v157, v69
	v_exp_f32_e32 v158, v70
	v_exp_f32_e32 v159, v71
	v_exp_f32_e32 v160, v72
	v_exp_f32_e32 v161, v73
	v_exp_f32_e32 v162, v74
	v_exp_f32_e32 v163, v75
	v_exp_f32_e32 v164, v76
	v_exp_f32_e32 v165, v77
	v_exp_f32_e32 v166, v78
	v_exp_f32_e32 v167, v79
	v_exp_f32_e32 v168, v80
	v_exp_f32_e32 v169, v81
	v_exp_f32_e32 v170, v82
	v_exp_f32_e32 v171, v83
	v_add_f32_e32 v249, v156, v157
	v_add_f32_e32 v250, v158, v159
	v_add_f32_e32 v249, v249, v160
	v_add_f32_e32 v250, v250, v161
	v_add_f32_e32 v249, v249, v162
	v_add_f32_e32 v250, v250, v163
	v_add_f32_e32 v249, v249, v164
	v_add_f32_e32 v250, v250, v165
	v_add_f32_e32 v249, v249, v166
	v_add_f32_e32 v250, v250, v167
	v_add_f32_e32 v249, v249, v168
	v_add_f32_e32 v250, v250, v169
	v_add_f32_e32 v249, v249, v170
	v_add_f32_e32 v250, v250, v171
	v_add_f32_e32 v249, v249, v250
	v_cvt_pk_bf16_f32 v156, v156, v157
	v_cvt_pk_bf16_f32 v157, v158, v159
	v_cvt_pk_bf16_f32 v158, v160, v161
	v_cvt_pk_bf16_f32 v159, v162, v163
	v_cvt_pk_bf16_f32 v160, v164, v165
	v_cvt_pk_bf16_f32 v161, v166, v167
	v_cvt_pk_bf16_f32 v162, v168, v169
	v_cvt_pk_bf16_f32 v163, v170, v171
	s_nop 1
	v_permlane32_swap_b32_e32 v156, v158
	v_permlane32_swap_b32_e32 v157, v159
	v_permlane32_swap_b32_e32 v160, v162
	v_permlane32_swap_b32_e32 v161, v163
	s_branch .Lsum_a1b0

.LBB0_1467:
	s_cmp_eq_u32 s99, 1
	s_cbranch_scc0 .Lorig_a1b1
	s_setprio 3
	ds_read_b128 v[140:143], v177
	ds_read_b128 v[144:147], v177 offset:32
	ds_read_b128 v[148:151], v177 offset:64
	ds_read_b128 v[152:155], v177 offset:96
	ds_read_b128 v[156:159], v177 offset:128
	ds_read_b128 v[160:163], v177 offset:160
	ds_read_b128 v[164:167], v177 offset:192
	ds_read_b128 v[168:171], v177 offset:224
	s_waitcnt lgkmcnt(4)
	v_mfma_f32_32x32x16_bf16 v[84:99], v[208:211], v[100:103], v[140:155]
	ds_read_b128 v[208:211], v172 offset:57344
	s_waitcnt lgkmcnt(15)
	v_mfma_f32_32x32x16_bf16 v[84:99], v[212:215], v[104:107], v[84:99]
	ds_read_b128 v[212:215], v206 offset:57344
	s_waitcnt lgkmcnt(15)
	v_mfma_f32_32x32x16_bf16 v[84:99], v[216:219], v[108:111], v[84:99]
	ds_read_b128 v[216:219], v207 offset:57344
	s_waitcnt lgkmcnt(15)
	v_mfma_f32_32x32x16_bf16 v[84:99], v[220:223], v[112:115], v[84:99]
	ds_read_b128 v[220:223], v237 offset:57344
	s_waitcnt lgkmcnt(15)
	v_mfma_f32_32x32x16_bf16 v[84:99], v[224:227], v[116:119], v[84:99]
	ds_read_b128 v[224:227], v244 offset:57344
	s_waitcnt lgkmcnt(15)
	v_mfma_f32_32x32x16_bf16 v[84:99], v[228:231], v[120:123], v[84:99]
	ds_read_b128 v[228:231], v245 offset:57344
	s_waitcnt lgkmcnt(15)
	v_mfma_f32_32x32x16_bf16 v[84:99], v[232:235], v[124:127], v[84:99]
	ds_read_b128 v[232:235], v246 offset:57344
	s_waitcnt lgkmcnt(15)
	v_mfma_f32_32x32x16_bf16 v[84:99], v[238:241], v[128:131], v[84:99]
	ds_read_b128 v[238:241], v247 offset:57344
	s_waitcnt lgkmcnt(7)
	v_mfma_f32_32x32x16_bf16 v[68:83], v[208:211], v[100:103], v[156:171]
	s_waitcnt lgkmcnt(6)
	v_mfma_f32_32x32x16_bf16 v[68:83], v[212:215], v[104:107], v[68:83]
	s_waitcnt lgkmcnt(5)
	v_mfma_f32_32x32x16_bf16 v[68:83], v[216:219], v[108:111], v[68:83]
	s_waitcnt lgkmcnt(4)
	v_mfma_f32_32x32x16_bf16 v[68:83], v[220:223], v[112:115], v[68:83]
	s_waitcnt lgkmcnt(3)
	v_mfma_f32_32x32x16_bf16 v[68:83], v[224:227], v[116:119], v[68:83]
	s_waitcnt lgkmcnt(2)
	v_mfma_f32_32x32x16_bf16 v[68:83], v[228:231], v[120:123], v[68:83]
	s_waitcnt lgkmcnt(1)
	v_mfma_f32_32x32x16_bf16 v[68:83], v[232:235], v[124:127], v[68:83]
	s_waitcnt lgkmcnt(0)
	v_mfma_f32_32x32x16_bf16 v[68:83], v[238:241], v[128:131], v[68:83]
	ds_read_b64_tr_b16 v[208:209], v174 offset:16384
	ds_read_b64_tr_b16 v[210:211], v174 offset:18432
	ds_read_b64_tr_b16 v[212:213], v174 offset:20480
	ds_read_b64_tr_b16 v[214:215], v174 offset:22528
	ds_read_b64_tr_b16 v[216:217], v174 offset:24576
	ds_read_b64_tr_b16 v[218:219], v174 offset:26624
	ds_read_b64_tr_b16 v[220:221], v174 offset:28672
	ds_read_b64_tr_b16 v[222:223], v174 offset:30720
	s_setprio 0
	s_nop 7
	s_nop 3
	v_cmp_eq_f32_e32 vcc, 0, v192
	s_cmp_eq_u64 vcc, exec
	s_cbranch_scc0 .Lsub_a1b1
	v_exp_f32_e32 v140, v84
	v_exp_f32_e32 v141, v85
	v_exp_f32_e32 v142, v86
	v_exp_f32_e32 v143, v87
	v_exp_f32_e32 v144, v88
	v_exp_f32_e32 v145, v89
	v_exp_f32_e32 v146, v90
	v_exp_f32_e32 v147, v91
	v_exp_f32_e32 v148, v92
	v_exp_f32_e32 v149, v93
	v_exp_f32_e32 v150, v94
	v_exp_f32_e32 v151, v95
	v_exp_f32_e32 v152, v96
	v_exp_f32_e32 v153, v97
	v_exp_f32_e32 v154, v98
	v_exp_f32_e32 v155, v99
	v_add_f32_e32 v248, v140, v141
	v_add_f32_e32 v250, v142, v143
	v_add_f32_e32 v248, v248, v144
	v_add_f32_e32 v250, v250, v145
	v_add_f32_e32 v248, v248, v146
	v_add_f32_e32 v250, v250, v147
	v_add_f32_e32 v248, v248, v148
	v_add_f32_e32 v250, v250, v149
	v_add_f32_e32 v248, v248, v150
	v_add_f32_e32 v250, v250, v151
	v_add_f32_e32 v248, v248, v152
	v_add_f32_e32 v250, v250, v153
	v_add_f32_e32 v248, v248, v154
	v_add_f32_e32 v250, v250, v155
	v_add_f32_e32 v248, v248, v250
	v_cvt_pk_bf16_f32 v140, v140, v141
	v_cvt_pk_bf16_f32 v141, v142, v143
	v_cvt_pk_bf16_f32 v142, v144, v145
	v_cvt_pk_bf16_f32 v143, v146, v147
	v_cvt_pk_bf16_f32 v144, v148, v149
	v_cvt_pk_bf16_f32 v145, v150, v151
	v_cvt_pk_bf16_f32 v146, v152, v153
	v_cvt_pk_bf16_f32 v147, v154, v155
	s_nop 1
	v_permlane32_swap_b32_e32 v140, v142
	v_permlane32_swap_b32_e32 v141, v143
	v_permlane32_swap_b32_e32 v144, v146
	v_permlane32_swap_b32_e32 v145, v147
	v_exp_f32_e32 v156, v68
	v_exp_f32_e32 v157, v69
	v_exp_f32_e32 v158, v70
	v_exp_f32_e32 v159, v71
	v_exp_f32_e32 v160, v72
	v_exp_f32_e32 v161, v73
	v_exp_f32_e32 v162, v74
	v_exp_f32_e32 v163, v75
	v_exp_f32_e32 v164, v76
	v_exp_f32_e32 v165, v77
	v_exp_f32_e32 v166, v78
	v_exp_f32_e32 v167, v79
	v_exp_f32_e32 v168, v80
	v_exp_f32_e32 v169, v81
	v_exp_f32_e32 v170, v82
	v_exp_f32_e32 v171, v83
	v_add_f32_e32 v249, v156, v157
	v_add_f32_e32 v250, v158, v159
	v_add_f32_e32 v249, v249, v160
	v_add_f32_e32 v250, v250, v161
	v_add_f32_e32 v249, v249, v162
	v_add_f32_e32 v250, v250, v163
	v_add_f32_e32 v249, v249, v164
	v_add_f32_e32 v250, v250, v165
	v_add_f32_e32 v249, v249, v166
	v_add_f32_e32 v250, v250, v167
	v_add_f32_e32 v249, v249, v168
	v_add_f32_e32 v250, v250, v169
	v_add_f32_e32 v249, v249, v170
	v_add_f32_e32 v250, v250, v171
	v_add_f32_e32 v249, v249, v250
	v_cvt_pk_bf16_f32 v156, v156, v157
	v_cvt_pk_bf16_f32 v157, v158, v159
	v_cvt_pk_bf16_f32 v158, v160, v161
	v_cvt_pk_bf16_f32 v159, v162, v163
	v_cvt_pk_bf16_f32 v160, v164, v165
	v_cvt_pk_bf16_f32 v161, v166, v167
	v_cvt_pk_bf16_f32 v162, v168, v169
	v_cvt_pk_bf16_f32 v163, v170, v171
	s_nop 1
	v_permlane32_swap_b32_e32 v156, v158
	v_permlane32_swap_b32_e32 v157, v159
	v_permlane32_swap_b32_e32 v160, v162
	v_permlane32_swap_b32_e32 v161, v163
	s_branch .Lsum_a1b1
